# v88 + accumulator zero-init removed: first K-iteration peeled in the three GEMM loops, first MFMA of each accumulator takes SrcC=0 (128 v_mov per unit gone)
# speedup vs baseline: 1.0057x; 1.0036x over previous
; #define PG8_STAGEA(bufoff, soff, voff) do { _Pragma("unroll") for (int _i = 0; _i < 2; ++_i) \
;         __builtin_amdgcn_raw_ptr_buffer_load_lds(rsA, (PG8_LAS unsigned*)(lds + (bufoff) + ldsw + _i * 8192), 16, (voff)[_i], (soff), 0, 0); } while (0)
; #define PG8_STAGEB(bufoff, soff, voff) do { _Pragma("unroll") for (int _i = 0; _i < 2; ++_i) \
;         __builtin_amdgcn_raw_ptr_buffer_load_lds(rsB, (PG8_LAS unsigned*)(lds + (bufoff) + ldsw + _i * 8192), 16, (voff)[_i], (soff), 0, 0); } while (0)
; #define PG8_LDA(dst, b, h) do { _Pragma("unroll") for (int m = 0; m < 4; ++m) _Pragma("unroll") for (int k = 0; k < 2; ++k) dst[m][k] = *(const PG8_LAS bf16x8*)(lds + PG8_SA(b, h) + aoff + m * 2048 + k * 1024); } while (0)
; #define PG8_LDB(dst, b, h) do { _Pragma("unroll") for (int n = 0; n < 2; ++n) _Pragma("unroll") for (int k = 0; k < 2; ++k) dst[n][k] = *(const PG8_LAS bf16x8*)(lds + PG8_SB(b, h) + boff + n * 2048 + k * 1024); } while (0)
; #define PG8_MMA(ai, bj, At, Bt) do { __builtin_amdgcn_s_setprio(1); _Pragma("unroll") for (int m = 0; m < 4; ++m) _Pragma("unroll") for (int n = 0; n < 2; ++n) _Pragma("unroll") for (int k = 0; k < 2; ++k) \
;         acc[ai][bj][m][n] = __builtin_amdgcn_mfma_f32_16x16x32_bf16(Bt[n][k], At[m][k], acc[ai][bj][m][n], 0, 0, 0); __builtin_amdgcn_s_setprio(0); } while (0)
; #define PG8_BAR __builtin_amdgcn_s_barrier()
; template <class Epi, class Sched, bool ALIGN_EPI = false>
; __device__ __forceinline__ void gemm_phase(PG8_LAS unsigned char* lds, const Gemm g, const Sched& S, const Epi& E, const int tid) {
;     ...
;             PG8_LDB(B0, 0, 0); PG8_LDB(B1, 0, 1); PG8_SCHED; PG8_LDA(At, 0, 0); PG8_STAGEA(PG8_SA(1, 1), a1 + hstepA, voffA);
;             PG8_WAIT_V(8); PG8_WAIT_L(0); PG8_BAR; PG8_MMA(0, 0, At, B0); PG8_MMA(0, 1, At, B1); PG8_BAR; PG8_SCHED;
;             PG8_LDA(At, 0, 1); PG8_STAGEB(PG8_SB(0, 0), b2, voffB); PG8_STAGEB(PG8_SB(0, 1), b2 + hstepB, voffB); PG8_STAGEA(PG8_SA(0, 0), a2, voffA);
;             PG8_WAIT_V(8); PG8_WAIT_L(0); PG8_BAR; PG8_MMA(1, 0, At, B0); PG8_MMA(1, 1, At, B1); PG8_BAR; PG8_SCHED;
;     ...
; #pragma unroll
;         for (int a = 0; a < 2; ++a)
; #pragma unroll
;             for (int b = 0; b < 2; ++b)
; #pragma unroll
;                 for (int m = 0; m < 4; ++m)
; #pragma unroll
;                     for (int n = 0; n < 2; ++n) acc[a][b][m][n] = (f32x4){0.f, 0.f, 0.f, 0.f};
.LBB0_306:
	s_lshl_b32 s33, s30, 20
	s_and_b64 s[18:19], s[42:43], exec
	s_cselect_b32 s18, s33, s37
	s_add_i32 s19, s37, 0x80080
	s_addk_i32 s36, 0x100
	s_mov_b32 s37, -2
	v_add_u32_e32 v130, 0x10000, v137
	ds_read_b128 v[144:147], v130
	ds_read_b128 v[148:151], v130 offset:1024
	ds_read_b128 v[164:167], v130 offset:2048
	ds_read_b128 v[168:171], v130 offset:3072
	v_add_u32_e32 v130, 0x14000, v137
	ds_read_b128 v[172:175], v130
	ds_read_b128 v[176:179], v130 offset:1024
	ds_read_b128 v[180:183], v130 offset:2048
	ds_read_b128 v[184:187], v130 offset:3072
	s_add_i32 s38, s19, 0xfff80080
	s_cmp_eq_u32 s37, 28
	s_cselect_b32 s42, s18, s38
	s_cselect_b32 s39, s31, s36
	s_or_b32 s38, s42, 0x80
	s_mov_b32 m0, s26
	ds_read_b128 v[188:191], v138
	ds_read_b128 v[202:205], v138 offset:1024
	ds_read_b128 v[206:209], v138 offset:2048
	ds_read_b128 v[210:213], v138 offset:3072
	ds_read_b128 v[214:217], v138 offset:4096
	ds_read_b128 v[218:221], v138 offset:5120
	ds_read_b128 v[222:225], v138 offset:6144
	ds_read_b128 v[226:229], v138 offset:7168
	buffer_load_dwordx4 v0, s[88:91], s19 offen lds
	s_mov_b32 m0, s27
	s_nop 0
	buffer_load_dwordx4 v133, s[88:91], s19 offen lds
	s_waitcnt vmcnt(8)
	s_waitcnt lgkmcnt(0)
	s_barrier
	s_setprio 1
	s_waitcnt lgkmcnt(7)
	v_mfma_f32_16x16x32_bf16 v[126:129], v[144:147], v[188:191], 0
	v_mfma_f32_16x16x32_bf16 v[118:121], v[164:167], v[188:191], 0
	s_waitcnt lgkmcnt(5)
	v_mfma_f32_16x16x32_bf16 v[110:113], v[144:147], v[206:209], 0
	v_mfma_f32_16x16x32_bf16 v[102:105], v[164:167], v[206:209], 0
	s_waitcnt lgkmcnt(3)
	v_mfma_f32_16x16x32_bf16 v[94:97], v[144:147], v[214:217], 0
	v_mfma_f32_16x16x32_bf16 v[86:89], v[164:167], v[214:217], 0
	s_waitcnt lgkmcnt(1)
	v_mfma_f32_16x16x32_bf16 v[78:81], v[144:147], v[222:225], 0
	v_mfma_f32_16x16x32_bf16 v[70:73], v[164:167], v[222:225], 0
	v_mfma_f32_16x16x32_bf16 v[126:129], v[148:151], v[202:205], v[126:129]
	v_mfma_f32_16x16x32_bf16 v[118:121], v[168:171], v[202:205], v[118:121]
	v_mfma_f32_16x16x32_bf16 v[110:113], v[148:151], v[210:213], v[110:113]
	v_mfma_f32_16x16x32_bf16 v[102:105], v[168:171], v[210:213], v[102:105]
	v_mfma_f32_16x16x32_bf16 v[94:97], v[148:151], v[218:221], v[94:97]
	v_mfma_f32_16x16x32_bf16 v[86:89], v[168:171], v[218:221], v[86:89]
	s_waitcnt lgkmcnt(0)
	v_mfma_f32_16x16x32_bf16 v[78:81], v[148:151], v[226:229], v[78:81]
	v_mfma_f32_16x16x32_bf16 v[70:73], v[168:171], v[226:229], v[70:73]
	s_setprio 0
	s_setprio 1
	v_mfma_f32_16x16x32_bf16 v[122:125], v[172:175], v[188:191], 0
	v_mfma_f32_16x16x32_bf16 v[114:117], v[180:183], v[188:191], 0
	v_mfma_f32_16x16x32_bf16 v[106:109], v[172:175], v[206:209], 0
	v_mfma_f32_16x16x32_bf16 v[98:101], v[180:183], v[206:209], 0
	v_mfma_f32_16x16x32_bf16 v[90:93], v[172:175], v[214:217], 0
	v_mfma_f32_16x16x32_bf16 v[82:85], v[180:183], v[214:217], 0
	v_mfma_f32_16x16x32_bf16 v[74:77], v[172:175], v[222:225], 0
	v_mfma_f32_16x16x32_bf16 v[66:69], v[180:183], v[222:225], 0
	v_mfma_f32_16x16x32_bf16 v[122:125], v[176:179], v[202:205], v[122:125]
	v_mfma_f32_16x16x32_bf16 v[114:117], v[184:187], v[202:205], v[114:117]
	v_mfma_f32_16x16x32_bf16 v[106:109], v[176:179], v[210:213], v[106:109]
	v_mfma_f32_16x16x32_bf16 v[98:101], v[184:187], v[210:213], v[98:101]
	v_mfma_f32_16x16x32_bf16 v[90:93], v[176:179], v[218:221], v[90:93]
	v_mfma_f32_16x16x32_bf16 v[82:85], v[184:187], v[218:221], v[82:85]
	v_mfma_f32_16x16x32_bf16 v[74:77], v[176:179], v[226:229], v[74:77]
	v_mfma_f32_16x16x32_bf16 v[66:69], v[184:187], v[226:229], v[66:69]
	s_setprio 0
	s_barrier
	s_mov_b32 m0, s3
	s_mov_b32 s46, s90
	s_mov_b32 s47, s91
	ds_read_b128 v[188:191], v138 offset:16384
	ds_read_b128 v[202:205], v138 offset:17408
	ds_read_b128 v[206:209], v138 offset:18432
	ds_read_b128 v[210:213], v138 offset:19456
	ds_read_b128 v[214:217], v138 offset:20480
	ds_read_b128 v[218:221], v138 offset:21504
	ds_read_b128 v[222:225], v138 offset:22528
	ds_read_b128 v[226:229], v138 offset:23552
	buffer_load_dwordx4 v132, s[44:47], s39 offen lds
	s_mov_b32 m0, s7
	s_add_i32 s43, s39, 0x80000
	buffer_load_dwordx4 v134, s[44:47], s39 offen lds
	s_mov_b32 m0, s11
	s_nop 0
	buffer_load_dwordx4 v132, s[44:47], s43 offen lds
	s_mov_b32 m0, s14
	s_nop 0
	buffer_load_dwordx4 v134, s[44:47], s43 offen lds
	s_mov_b32 m0, s2
	s_nop 0
	buffer_load_dwordx4 v0, s[88:91], s42 offen lds
	s_mov_b32 m0, s15
	s_nop 0
	buffer_load_dwordx4 v133, s[88:91], s42 offen lds
	s_waitcnt vmcnt(8)
	s_waitcnt lgkmcnt(0)
	s_barrier
	s_setprio 1
	s_waitcnt lgkmcnt(7)
	v_mfma_f32_16x16x32_bf16 v[62:65], v[144:147], v[188:191], 0
	v_mfma_f32_16x16x32_bf16 v[54:57], v[164:167], v[188:191], 0
	s_waitcnt lgkmcnt(5)
	v_mfma_f32_16x16x32_bf16 v[46:49], v[144:147], v[206:209], 0
	v_mfma_f32_16x16x32_bf16 v[38:41], v[164:167], v[206:209], 0
	s_waitcnt lgkmcnt(3)
	v_mfma_f32_16x16x32_bf16 v[30:33], v[144:147], v[214:217], 0
	v_mfma_f32_16x16x32_bf16 v[22:25], v[164:167], v[214:217], 0
	s_waitcnt lgkmcnt(1)
	v_mfma_f32_16x16x32_bf16 v[14:17], v[144:147], v[222:225], 0
	v_mfma_f32_16x16x32_bf16 v[6:9], v[164:167], v[222:225], 0
	v_mfma_f32_16x16x32_bf16 v[62:65], v[148:151], v[202:205], v[62:65]
	v_mfma_f32_16x16x32_bf16 v[54:57], v[168:171], v[202:205], v[54:57]
	v_mfma_f32_16x16x32_bf16 v[46:49], v[148:151], v[210:213], v[46:49]
	v_mfma_f32_16x16x32_bf16 v[38:41], v[168:171], v[210:213], v[38:41]
	v_mfma_f32_16x16x32_bf16 v[30:33], v[148:151], v[218:221], v[30:33]
	v_mfma_f32_16x16x32_bf16 v[22:25], v[168:171], v[218:221], v[22:25]
	s_waitcnt lgkmcnt(0)
	v_mfma_f32_16x16x32_bf16 v[14:17], v[148:151], v[226:229], v[14:17]
	v_mfma_f32_16x16x32_bf16 v[6:9], v[168:171], v[226:229], v[6:9]
	s_setprio 0
	s_setprio 1
	v_mfma_f32_16x16x32_bf16 v[58:61], v[172:175], v[188:191], 0
	v_mfma_f32_16x16x32_bf16 v[50:53], v[180:183], v[188:191], 0
	v_mfma_f32_16x16x32_bf16 v[42:45], v[172:175], v[206:209], 0
	v_mfma_f32_16x16x32_bf16 v[34:37], v[180:183], v[206:209], 0
	v_mfma_f32_16x16x32_bf16 v[26:29], v[172:175], v[214:217], 0
	v_mfma_f32_16x16x32_bf16 v[18:21], v[180:183], v[214:217], 0
	v_mfma_f32_16x16x32_bf16 v[10:13], v[172:175], v[222:225], 0
	v_mfma_f32_16x16x32_bf16 v[2:5], v[180:183], v[222:225], 0
	v_mfma_f32_16x16x32_bf16 v[58:61], v[176:179], v[202:205], v[58:61]
	v_mfma_f32_16x16x32_bf16 v[50:53], v[184:187], v[202:205], v[50:53]
	v_mfma_f32_16x16x32_bf16 v[42:45], v[176:179], v[210:213], v[42:45]
	v_mfma_f32_16x16x32_bf16 v[34:37], v[184:187], v[210:213], v[34:37]
	v_mfma_f32_16x16x32_bf16 v[26:29], v[176:179], v[218:221], v[26:29]
	v_mfma_f32_16x16x32_bf16 v[18:21], v[184:187], v[218:221], v[18:21]
	v_mfma_f32_16x16x32_bf16 v[10:13], v[176:179], v[226:229], v[10:13]
	v_mfma_f32_16x16x32_bf16 v[2:5], v[184:187], v[226:229], v[2:5]
	s_setprio 0
	s_barrier
; #define PG8_STAGEA(bufoff, soff, voff) do { _Pragma("unroll") for (int _i = 0; _i < 2; ++_i) \
;         __builtin_amdgcn_raw_ptr_buffer_load_lds(rsA, (PG8_LAS unsigned*)(lds + (bufoff) + ldsw + _i * 8192), 16, (voff)[_i], (soff), 0, 0); } while (0)
; #define PG8_STAGEB(bufoff, soff, voff) do { _Pragma("unroll") for (int _i = 0; _i < 2; ++_i) \
;         __builtin_amdgcn_raw_ptr_buffer_load_lds(rsB, (PG8_LAS unsigned*)(lds + (bufoff) + ldsw + _i * 8192), 16, (voff)[_i], (soff), 0, 0); } while (0)
; #define PG8_LDA(dst, b, h) do { _Pragma("unroll") for (int m = 0; m < 4; ++m) _Pragma("unroll") for (int k = 0; k < 2; ++k) dst[m][k] = *(const PG8_LAS bf16x8*)(lds + PG8_SA(b, h) + aoff + m * 2048 + k * 1024); } while (0)
; #define PG8_LDB(dst, b, h) do { _Pragma("unroll") for (int n = 0; n < 2; ++n) _Pragma("unroll") for (int k = 0; k < 2; ++k) dst[n][k] = *(const PG8_LAS bf16x8*)(lds + PG8_SB(b, h) + boff + n * 2048 + k * 1024); } while (0)
; #define PG8_MMA(ai, bj, At, Bt) do { __builtin_amdgcn_s_setprio(1); _Pragma("unroll") for (int m = 0; m < 4; ++m) _Pragma("unroll") for (int n = 0; n < 2; ++n) _Pragma("unroll") for (int k = 0; k < 2; ++k) \
;         acc[ai][bj][m][n] = __builtin_amdgcn_mfma_f32_16x16x32_bf16(Bt[n][k], At[m][k], acc[ai][bj][m][n], 0, 0, 0); __builtin_amdgcn_s_setprio(0); } while (0)
; #define PG8_WAIT_V(n) asm volatile("s_waitcnt vmcnt(" #n ")" ::: "memory")
; #define PG8_WAIT_L(n) asm volatile("s_waitcnt lgkmcnt(" #n ")" ::: "memory")
; #define PG8_BAR __builtin_amdgcn_s_barrier()
; #define PG8_SCHED __builtin_amdgcn_sched_barrier(0)
; template <class Epi, class Sched, bool ALIGN_EPI = false>
; __device__ __forceinline__ void gemm_phase(PG8_LAS unsigned char* lds, const Gemm g, const Sched& S, const Epi& E, const int tid) {
;     ...
;             PG8_LDB(B0, 1, 0); PG8_LDB(B1, 1, 1); PG8_SCHED; PG8_LDA(At, 1, 0); PG8_STAGEA(PG8_SA(0, 1), a2 + hstepA, voffA);
;             PG8_WAIT_V(8); PG8_WAIT_L(0); PG8_BAR; PG8_MMA(0, 0, At, B0); PG8_MMA(0, 1, At, B1); PG8_BAR; PG8_SCHED;
;             PG8_LDA(At, 1, 1); PG8_STAGEB(PG8_SB(1, 0), b3, voffB); PG8_STAGEB(PG8_SB(1, 1), b3 + hstepB, voffB); PG8_STAGEA(PG8_SA(1, 0), a3, voffA);
;             PG8_WAIT_V(8); PG8_WAIT_L(0); PG8_BAR; PG8_MMA(1, 0, At, B0); PG8_MMA(1, 1, At, B1); PG8_BAR; PG8_SCHED;
	v_add_u32_e32 v130, 0x18000, v137
	ds_read_b128 v[144:147], v130
	ds_read_b128 v[148:151], v130 offset:1024
	ds_read_b128 v[164:167], v130 offset:2048
	ds_read_b128 v[168:171], v130 offset:3072
	v_add_u32_e32 v130, 0x1c000, v137
	ds_read_b128 v[172:175], v130
	ds_read_b128 v[176:179], v130 offset:1024
	ds_read_b128 v[180:183], v130 offset:2048
	ds_read_b128 v[184:187], v130 offset:3072
	s_add_i32 s42, s42, 0x80000
	s_mov_b32 m0, s16
	ds_read_b128 v[188:191], v138 offset:32768
	ds_read_b128 v[202:205], v138 offset:33792
	ds_read_b128 v[206:209], v138 offset:34816
	ds_read_b128 v[210:213], v138 offset:35840
	ds_read_b128 v[214:217], v138 offset:36864
	ds_read_b128 v[218:221], v138 offset:37888
	ds_read_b128 v[222:225], v138 offset:38912
	ds_read_b128 v[226:229], v138 offset:39936
	buffer_load_dwordx4 v0, s[88:91], s42 offen lds
	s_mov_b32 m0, s17
	s_nop 0
	buffer_load_dwordx4 v133, s[88:91], s42 offen lds
	s_waitcnt vmcnt(8)
	s_waitcnt lgkmcnt(0)
	s_barrier
	s_setprio 1
	s_waitcnt lgkmcnt(7)
	v_mfma_f32_16x16x32_bf16 v[126:129], v[144:147], v[188:191], v[126:129]
	v_mfma_f32_16x16x32_bf16 v[118:121], v[164:167], v[188:191], v[118:121]
	s_waitcnt lgkmcnt(5)
	v_mfma_f32_16x16x32_bf16 v[110:113], v[144:147], v[206:209], v[110:113]
	v_mfma_f32_16x16x32_bf16 v[102:105], v[164:167], v[206:209], v[102:105]
	s_waitcnt lgkmcnt(3)
	v_mfma_f32_16x16x32_bf16 v[94:97], v[144:147], v[214:217], v[94:97]
	v_mfma_f32_16x16x32_bf16 v[86:89], v[164:167], v[214:217], v[86:89]
	s_waitcnt lgkmcnt(1)
	v_mfma_f32_16x16x32_bf16 v[78:81], v[144:147], v[222:225], v[78:81]
	v_mfma_f32_16x16x32_bf16 v[70:73], v[164:167], v[222:225], v[70:73]
	v_mfma_f32_16x16x32_bf16 v[126:129], v[148:151], v[202:205], v[126:129]
	v_mfma_f32_16x16x32_bf16 v[118:121], v[168:171], v[202:205], v[118:121]
	v_mfma_f32_16x16x32_bf16 v[110:113], v[148:151], v[210:213], v[110:113]
	v_mfma_f32_16x16x32_bf16 v[102:105], v[168:171], v[210:213], v[102:105]
	v_mfma_f32_16x16x32_bf16 v[94:97], v[148:151], v[218:221], v[94:97]
	v_mfma_f32_16x16x32_bf16 v[86:89], v[168:171], v[218:221], v[86:89]
	s_waitcnt lgkmcnt(0)
	v_mfma_f32_16x16x32_bf16 v[78:81], v[148:151], v[226:229], v[78:81]
	v_mfma_f32_16x16x32_bf16 v[70:73], v[168:171], v[226:229], v[70:73]
	s_setprio 0
	s_setprio 1
	v_mfma_f32_16x16x32_bf16 v[122:125], v[172:175], v[188:191], v[122:125]
	v_mfma_f32_16x16x32_bf16 v[114:117], v[180:183], v[188:191], v[114:117]
	v_mfma_f32_16x16x32_bf16 v[106:109], v[172:175], v[206:209], v[106:109]
	v_mfma_f32_16x16x32_bf16 v[98:101], v[180:183], v[206:209], v[98:101]
	v_mfma_f32_16x16x32_bf16 v[90:93], v[172:175], v[214:217], v[90:93]
	v_mfma_f32_16x16x32_bf16 v[82:85], v[180:183], v[214:217], v[82:85]
	v_mfma_f32_16x16x32_bf16 v[74:77], v[172:175], v[222:225], v[74:77]
	v_mfma_f32_16x16x32_bf16 v[66:69], v[180:183], v[222:225], v[66:69]
	v_mfma_f32_16x16x32_bf16 v[122:125], v[176:179], v[202:205], v[122:125]
	v_mfma_f32_16x16x32_bf16 v[114:117], v[184:187], v[202:205], v[114:117]
	v_mfma_f32_16x16x32_bf16 v[106:109], v[176:179], v[210:213], v[106:109]
	v_mfma_f32_16x16x32_bf16 v[98:101], v[184:187], v[210:213], v[98:101]
	v_mfma_f32_16x16x32_bf16 v[90:93], v[176:179], v[218:221], v[90:93]
	v_mfma_f32_16x16x32_bf16 v[82:85], v[184:187], v[218:221], v[82:85]
	v_mfma_f32_16x16x32_bf16 v[74:77], v[176:179], v[226:229], v[74:77]
	v_mfma_f32_16x16x32_bf16 v[66:69], v[184:187], v[226:229], v[66:69]
	s_setprio 0
	s_barrier
	s_mov_b32 m0, s20
	s_or_b32 s42, s39, 0x80
	ds_read_b128 v[188:191], v138 offset:49152
	ds_read_b128 v[202:205], v138 offset:50176
	ds_read_b128 v[206:209], v138 offset:51200
	ds_read_b128 v[210:213], v138 offset:52224
	ds_read_b128 v[214:217], v138 offset:53248
	ds_read_b128 v[218:221], v138 offset:54272
	ds_read_b128 v[222:225], v138 offset:55296
	ds_read_b128 v[226:229], v138 offset:56320
	buffer_load_dwordx4 v132, s[44:47], s42 offen lds
	s_mov_b32 m0, s21
	s_add_i32 s39, s39, 0x80080
	buffer_load_dwordx4 v134, s[44:47], s42 offen lds
	s_mov_b32 m0, s24
	s_nop 0
	buffer_load_dwordx4 v132, s[44:47], s39 offen lds
	s_mov_b32 m0, s25
	s_nop 0
	buffer_load_dwordx4 v134, s[44:47], s39 offen lds
	s_mov_b32 m0, s22
	s_nop 0
	buffer_load_dwordx4 v0, s[88:91], s38 offen lds
	s_mov_b32 m0, s23
	s_nop 0
	buffer_load_dwordx4 v133, s[88:91], s38 offen lds
	s_waitcnt vmcnt(8)
	s_waitcnt lgkmcnt(0)
	s_barrier
	s_setprio 1
	s_waitcnt lgkmcnt(7)
	v_mfma_f32_16x16x32_bf16 v[62:65], v[144:147], v[188:191], v[62:65]
	v_mfma_f32_16x16x32_bf16 v[54:57], v[164:167], v[188:191], v[54:57]
	s_waitcnt lgkmcnt(5)
	v_mfma_f32_16x16x32_bf16 v[46:49], v[144:147], v[206:209], v[46:49]
	v_mfma_f32_16x16x32_bf16 v[38:41], v[164:167], v[206:209], v[38:41]
	s_waitcnt lgkmcnt(3)
	v_mfma_f32_16x16x32_bf16 v[30:33], v[144:147], v[214:217], v[30:33]
	v_mfma_f32_16x16x32_bf16 v[22:25], v[164:167], v[214:217], v[22:25]
	s_waitcnt lgkmcnt(1)
	v_mfma_f32_16x16x32_bf16 v[14:17], v[144:147], v[222:225], v[14:17]
	v_mfma_f32_16x16x32_bf16 v[6:9], v[164:167], v[222:225], v[6:9]
	v_mfma_f32_16x16x32_bf16 v[62:65], v[148:151], v[202:205], v[62:65]
	v_mfma_f32_16x16x32_bf16 v[54:57], v[168:171], v[202:205], v[54:57]
	v_mfma_f32_16x16x32_bf16 v[46:49], v[148:151], v[210:213], v[46:49]
	v_mfma_f32_16x16x32_bf16 v[38:41], v[168:171], v[210:213], v[38:41]
	v_mfma_f32_16x16x32_bf16 v[30:33], v[148:151], v[218:221], v[30:33]
	v_mfma_f32_16x16x32_bf16 v[22:25], v[168:171], v[218:221], v[22:25]
	s_waitcnt lgkmcnt(0)
	v_mfma_f32_16x16x32_bf16 v[14:17], v[148:151], v[226:229], v[14:17]
	v_mfma_f32_16x16x32_bf16 v[6:9], v[168:171], v[226:229], v[6:9]
	s_setprio 0
	s_setprio 1
	v_mfma_f32_16x16x32_bf16 v[58:61], v[172:175], v[188:191], v[58:61]
	v_mfma_f32_16x16x32_bf16 v[50:53], v[180:183], v[188:191], v[50:53]
	v_mfma_f32_16x16x32_bf16 v[42:45], v[172:175], v[206:209], v[42:45]
	v_mfma_f32_16x16x32_bf16 v[34:37], v[180:183], v[206:209], v[34:37]
	v_mfma_f32_16x16x32_bf16 v[26:29], v[172:175], v[214:217], v[26:29]
	v_mfma_f32_16x16x32_bf16 v[18:21], v[180:183], v[214:217], v[18:21]
	v_mfma_f32_16x16x32_bf16 v[10:13], v[172:175], v[222:225], v[10:13]
	v_mfma_f32_16x16x32_bf16 v[2:5], v[180:183], v[222:225], v[2:5]
	v_mfma_f32_16x16x32_bf16 v[58:61], v[176:179], v[202:205], v[58:61]
	v_mfma_f32_16x16x32_bf16 v[50:53], v[184:187], v[202:205], v[50:53]
	v_mfma_f32_16x16x32_bf16 v[42:45], v[176:179], v[210:213], v[42:45]
	v_mfma_f32_16x16x32_bf16 v[34:37], v[184:187], v[210:213], v[34:37]
	v_mfma_f32_16x16x32_bf16 v[26:29], v[176:179], v[218:221], v[26:29]
	v_mfma_f32_16x16x32_bf16 v[18:21], v[184:187], v[218:221], v[18:21]
	v_mfma_f32_16x16x32_bf16 v[10:13], v[176:179], v[226:229], v[10:13]
	v_mfma_f32_16x16x32_bf16 v[2:5], v[184:187], v[226:229], v[2:5]
	s_setprio 0
	s_barrier
	s_add_i32 s37, s37, 2
	s_addk_i32 s19, 0x100
	s_addk_i32 s36, 0x100
	s_cmp_gt_u32 s37, 29

; #define PG8_STAGEA(bufoff, soff, voff) do { _Pragma("unroll") for (int _i = 0; _i < 2; ++_i) \
;         __builtin_amdgcn_raw_ptr_buffer_load_lds(rsA, (PG8_LAS unsigned*)(lds + (bufoff) + ldsw + _i * 8192), 16, (voff)[_i], (soff), 0, 0); } while (0)
; #define PG8_STAGEB(bufoff, soff, voff) do { _Pragma("unroll") for (int _i = 0; _i < 2; ++_i) \
;         __builtin_amdgcn_raw_ptr_buffer_load_lds(rsB, (PG8_LAS unsigned*)(lds + (bufoff) + ldsw + _i * 8192), 16, (voff)[_i], (soff), 0, 0); } while (0)
; #define PG8_LDA(dst, b, h) do { _Pragma("unroll") for (int m = 0; m < 4; ++m) _Pragma("unroll") for (int k = 0; k < 2; ++k) dst[m][k] = *(const PG8_LAS bf16x8*)(lds + PG8_SA(b, h) + aoff + m * 2048 + k * 1024); } while (0)
; #define PG8_LDB(dst, b, h) do { _Pragma("unroll") for (int n = 0; n < 2; ++n) _Pragma("unroll") for (int k = 0; k < 2; ++k) dst[n][k] = *(const PG8_LAS bf16x8*)(lds + PG8_SB(b, h) + boff + n * 2048 + k * 1024); } while (0)
; #define PG8_MMA(ai, bj, At, Bt) do { __builtin_amdgcn_s_setprio(1); _Pragma("unroll") for (int m = 0; m < 4; ++m) _Pragma("unroll") for (int n = 0; n < 2; ++n) _Pragma("unroll") for (int k = 0; k < 2; ++k) \
;         acc[ai][bj][m][n] = __builtin_amdgcn_mfma_f32_16x16x32_bf16(Bt[n][k], At[m][k], acc[ai][bj][m][n], 0, 0, 0); __builtin_amdgcn_s_setprio(0); } while (0)
; #define PG8_BAR __builtin_amdgcn_s_barrier()
; template <class Epi, class Sched, bool ALIGN_EPI = false>
; __device__ __forceinline__ void gemm_phase(PG8_LAS unsigned char* lds, const Gemm g, const Sched& S, const Epi& E, const int tid) {
;     ...
;             PG8_LDB(B0, 0, 0); PG8_LDB(B1, 0, 1); PG8_SCHED; PG8_LDA(At, 0, 0); PG8_STAGEA(PG8_SA(1, 1), a1 + hstepA, voffA);
;             PG8_WAIT_V(8); PG8_WAIT_L(0); PG8_BAR; PG8_MMA(0, 0, At, B0); PG8_MMA(0, 1, At, B1); PG8_BAR; PG8_SCHED;
;             PG8_LDA(At, 0, 1); PG8_STAGEB(PG8_SB(0, 0), b2, voffB); PG8_STAGEB(PG8_SB(0, 1), b2 + hstepB, voffB); PG8_STAGEA(PG8_SA(0, 0), a2, voffA);
;             PG8_WAIT_V(8); PG8_WAIT_L(0); PG8_BAR; PG8_MMA(1, 0, At, B0); PG8_MMA(1, 1, At, B1); PG8_BAR; PG8_SCHED;
;     ...
; #pragma unroll
;         for (int a = 0; a < 2; ++a)
; #pragma unroll
;             for (int b = 0; b < 2; ++b)
; #pragma unroll
;                 for (int m = 0; m < 4; ++m)
; #pragma unroll
;                     for (int n = 0; n < 2; ++n) acc[a][b][m][n] = (f32x4){0.f, 0.f, 0.f, 0.f};
.LBB0_329:
	s_lshl_b32 s59, s11, 20
	s_and_b64 s[0:1], s[44:45], exec
	s_waitcnt vmcnt(23)
	s_cselect_b32 s0, s59, s13
	s_add_i32 s1, s13, 0x80080
	s_addk_i32 s12, 0x100
	s_mov_b32 s13, -2
	s_waitcnt vmcnt(22)
	s_waitcnt vmcnt(19)
	s_waitcnt vmcnt(18)
	s_waitcnt vmcnt(14)
	v_add_u32_e32 v0, 0x10000, v170
	ds_read_b128 v[130:133], v0
	ds_read_b128 v[134:137], v0 offset:1024
	ds_read_b128 v[138:141], v0 offset:2048
	ds_read_b128 v[150:153], v0 offset:3072
	v_add_u32_e32 v0, 0x14000, v170
	ds_read_b128 v[172:175], v0
	ds_read_b128 v[176:179], v0 offset:1024
	ds_read_b128 v[180:183], v0 offset:2048
	ds_read_b128 v[184:187], v0 offset:3072
	s_add_i32 s14, s1, 0xfff80080
	s_cmp_eq_u32 s13, 28
	s_cselect_b32 s16, s0, s14
	s_cselect_b32 s15, s58, s12
	s_or_b32 s14, s16, 0x80
	s_mov_b32 m0, s54
	ds_read_b128 v[188:191], v171
	ds_read_b128 v[202:205], v171 offset:1024
	ds_read_b128 v[206:209], v171 offset:2048
	ds_read_b128 v[210:213], v171 offset:3072
	ds_read_b128 v[214:217], v171 offset:4096
	ds_read_b128 v[218:221], v171 offset:5120
	ds_read_b128 v[222:225], v171 offset:6144
	ds_read_b128 v[226:229], v171 offset:7168
	buffer_load_dwordx4 v145, s[88:91], s1 offen lds
	s_mov_b32 m0, s55
	s_nop 0
	buffer_load_dwordx4 v167, s[88:91], s1 offen lds
	s_waitcnt vmcnt(8)
	s_waitcnt lgkmcnt(0)
	s_barrier
	s_setprio 1
	s_waitcnt lgkmcnt(7)
	v_mfma_f32_16x16x32_bf16 v[118:121], v[130:133], v[188:191], 0
	v_mfma_f32_16x16x32_bf16 v[102:105], v[138:141], v[188:191], 0
	s_waitcnt lgkmcnt(5)
	v_mfma_f32_16x16x32_bf16 v[114:117], v[130:133], v[206:209], 0
	v_mfma_f32_16x16x32_bf16 v[98:101], v[138:141], v[206:209], 0
	s_waitcnt lgkmcnt(3)
	v_mfma_f32_16x16x32_bf16 v[86:89], v[130:133], v[214:217], 0
	v_mfma_f32_16x16x32_bf16 v[70:73], v[138:141], v[214:217], 0
	s_waitcnt lgkmcnt(1)
	v_mfma_f32_16x16x32_bf16 v[82:85], v[130:133], v[222:225], 0
	v_mfma_f32_16x16x32_bf16 v[66:69], v[138:141], v[222:225], 0
	v_mfma_f32_16x16x32_bf16 v[118:121], v[134:137], v[202:205], v[118:121]
	v_mfma_f32_16x16x32_bf16 v[102:105], v[150:153], v[202:205], v[102:105]
	v_mfma_f32_16x16x32_bf16 v[114:117], v[134:137], v[210:213], v[114:117]
	v_mfma_f32_16x16x32_bf16 v[98:101], v[150:153], v[210:213], v[98:101]
	v_mfma_f32_16x16x32_bf16 v[86:89], v[134:137], v[218:221], v[86:89]
	v_mfma_f32_16x16x32_bf16 v[70:73], v[150:153], v[218:221], v[70:73]
	s_waitcnt lgkmcnt(0)
	v_mfma_f32_16x16x32_bf16 v[82:85], v[134:137], v[226:229], v[82:85]
	v_mfma_f32_16x16x32_bf16 v[66:69], v[150:153], v[226:229], v[66:69]
	s_setprio 0
	s_setprio 1
	v_mfma_f32_16x16x32_bf16 v[126:129], v[172:175], v[188:191], 0
	v_mfma_f32_16x16x32_bf16 v[110:113], v[180:183], v[188:191], 0
	v_mfma_f32_16x16x32_bf16 v[122:125], v[172:175], v[206:209], 0
	v_mfma_f32_16x16x32_bf16 v[106:109], v[180:183], v[206:209], 0
	v_mfma_f32_16x16x32_bf16 v[94:97], v[172:175], v[214:217], 0
	v_mfma_f32_16x16x32_bf16 v[78:81], v[180:183], v[214:217], 0
	v_mfma_f32_16x16x32_bf16 v[90:93], v[172:175], v[222:225], 0
	v_mfma_f32_16x16x32_bf16 v[74:77], v[180:183], v[222:225], 0
	v_mfma_f32_16x16x32_bf16 v[126:129], v[176:179], v[202:205], v[126:129]
	v_mfma_f32_16x16x32_bf16 v[110:113], v[184:187], v[202:205], v[110:113]
	v_mfma_f32_16x16x32_bf16 v[122:125], v[176:179], v[210:213], v[122:125]
	v_mfma_f32_16x16x32_bf16 v[106:109], v[184:187], v[210:213], v[106:109]
	v_mfma_f32_16x16x32_bf16 v[94:97], v[176:179], v[218:221], v[94:97]
	v_mfma_f32_16x16x32_bf16 v[78:81], v[184:187], v[218:221], v[78:81]
	v_mfma_f32_16x16x32_bf16 v[90:93], v[176:179], v[226:229], v[90:93]
	v_mfma_f32_16x16x32_bf16 v[74:77], v[184:187], v[226:229], v[74:77]
	s_setprio 0
	s_barrier
	s_mov_b32 m0, s28
	s_mov_b32 s50, s90
	s_mov_b32 s51, s91
	ds_read_b128 v[188:191], v171 offset:16384
	ds_read_b128 v[202:205], v171 offset:17408
	ds_read_b128 v[206:209], v171 offset:18432
	ds_read_b128 v[210:213], v171 offset:19456
	ds_read_b128 v[214:217], v171 offset:20480
	ds_read_b128 v[218:221], v171 offset:21504
	ds_read_b128 v[222:225], v171 offset:22528
	ds_read_b128 v[226:229], v171 offset:23552
	buffer_load_dwordx4 v166, s[48:51], s15 offen lds
	s_mov_b32 m0, s29
	s_add_i32 s17, s15, 0x80000
	buffer_load_dwordx4 v168, s[48:51], s15 offen lds
	s_mov_b32 m0, s70
	s_nop 0
	buffer_load_dwordx4 v166, s[48:51], s17 offen lds
	s_mov_b32 m0, s71
	s_nop 0
	buffer_load_dwordx4 v168, s[48:51], s17 offen lds
	s_mov_b32 m0, s27
	s_nop 0
	buffer_load_dwordx4 v145, s[88:91], s16 offen lds
	s_mov_b32 m0, s72
	s_nop 0
	buffer_load_dwordx4 v167, s[88:91], s16 offen lds
	s_waitcnt vmcnt(8)
	s_waitcnt lgkmcnt(0)
	s_barrier
; #define PG8_STAGEA(bufoff, soff, voff) do { _Pragma("unroll") for (int _i = 0; _i < 2; ++_i) \
;         __builtin_amdgcn_raw_ptr_buffer_load_lds(rsA, (PG8_LAS unsigned*)(lds + (bufoff) + ldsw + _i * 8192), 16, (voff)[_i], (soff), 0, 0); } while (0)
; #define PG8_STAGEB(bufoff, soff, voff) do { _Pragma("unroll") for (int _i = 0; _i < 2; ++_i) \
;         __builtin_amdgcn_raw_ptr_buffer_load_lds(rsB, (PG8_LAS unsigned*)(lds + (bufoff) + ldsw + _i * 8192), 16, (voff)[_i], (soff), 0, 0); } while (0)
; #define PG8_LDA(dst, b, h) do { _Pragma("unroll") for (int m = 0; m < 4; ++m) _Pragma("unroll") for (int k = 0; k < 2; ++k) dst[m][k] = *(const PG8_LAS bf16x8*)(lds + PG8_SA(b, h) + aoff + m * 2048 + k * 1024); } while (0)
; #define PG8_LDB(dst, b, h) do { _Pragma("unroll") for (int n = 0; n < 2; ++n) _Pragma("unroll") for (int k = 0; k < 2; ++k) dst[n][k] = *(const PG8_LAS bf16x8*)(lds + PG8_SB(b, h) + boff + n * 2048 + k * 1024); } while (0)
; #define PG8_MMA(ai, bj, At, Bt) do { __builtin_amdgcn_s_setprio(1); _Pragma("unroll") for (int m = 0; m < 4; ++m) _Pragma("unroll") for (int n = 0; n < 2; ++n) _Pragma("unroll") for (int k = 0; k < 2; ++k) \
;         acc[ai][bj][m][n] = __builtin_amdgcn_mfma_f32_16x16x32_bf16(Bt[n][k], At[m][k], acc[ai][bj][m][n], 0, 0, 0); __builtin_amdgcn_s_setprio(0); } while (0)
; #define PG8_WAIT_V(n) asm volatile("s_waitcnt vmcnt(" #n ")" ::: "memory")
; #define PG8_WAIT_L(n) asm volatile("s_waitcnt lgkmcnt(" #n ")" ::: "memory")
; #define PG8_BAR __builtin_amdgcn_s_barrier()
; template <class Epi, class Sched, bool ALIGN_EPI = false>
; __device__ __forceinline__ void gemm_phase(PG8_LAS unsigned char* lds, const Gemm g, const Sched& S, const Epi& E, const int tid) {
;     ...
;             PG8_WAIT_V(8); PG8_WAIT_L(0); PG8_BAR; PG8_MMA(0, 0, At, B0); PG8_MMA(0, 1, At, B1); PG8_BAR; PG8_SCHED;
;             PG8_LDA(At, 0, 1); PG8_STAGEB(PG8_SB(0, 0), b2, voffB); PG8_STAGEB(PG8_SB(0, 1), b2 + hstepB, voffB); PG8_STAGEA(PG8_SA(0, 0), a2, voffA);
;             PG8_WAIT_V(8); PG8_WAIT_L(0); PG8_BAR; PG8_MMA(1, 0, At, B0); PG8_MMA(1, 1, At, B1); PG8_BAR; PG8_SCHED;
;             PG8_LDB(B0, 1, 0); PG8_LDB(B1, 1, 1); PG8_SCHED; PG8_LDA(At, 1, 0); PG8_STAGEA(PG8_SA(0, 1), a2 + hstepA, voffA);
;             PG8_WAIT_V(8); PG8_WAIT_L(0); PG8_BAR; PG8_MMA(0, 0, At, B0); PG8_MMA(0, 1, At, B1); PG8_BAR; PG8_SCHED;
	s_setprio 1
	s_waitcnt lgkmcnt(7)
	v_mfma_f32_16x16x32_bf16 v[54:57], v[130:133], v[188:191], 0
	v_mfma_f32_16x16x32_bf16 v[38:41], v[138:141], v[188:191], 0
	s_waitcnt lgkmcnt(5)
	v_mfma_f32_16x16x32_bf16 v[50:53], v[130:133], v[206:209], 0
	v_mfma_f32_16x16x32_bf16 v[34:37], v[138:141], v[206:209], 0
	s_waitcnt lgkmcnt(3)
	v_mfma_f32_16x16x32_bf16 v[22:25], v[130:133], v[214:217], 0
	v_mfma_f32_16x16x32_bf16 v[6:9], v[138:141], v[214:217], 0
	s_waitcnt lgkmcnt(1)
	v_mfma_f32_16x16x32_bf16 v[18:21], v[130:133], v[222:225], 0
	v_mfma_f32_16x16x32_bf16 v[2:5], v[138:141], v[222:225], 0
	v_mfma_f32_16x16x32_bf16 v[54:57], v[134:137], v[202:205], v[54:57]
	v_mfma_f32_16x16x32_bf16 v[38:41], v[150:153], v[202:205], v[38:41]
	v_mfma_f32_16x16x32_bf16 v[50:53], v[134:137], v[210:213], v[50:53]
	v_mfma_f32_16x16x32_bf16 v[34:37], v[150:153], v[210:213], v[34:37]
	v_mfma_f32_16x16x32_bf16 v[22:25], v[134:137], v[218:221], v[22:25]
	v_mfma_f32_16x16x32_bf16 v[6:9], v[150:153], v[218:221], v[6:9]
	s_waitcnt lgkmcnt(0)
	v_mfma_f32_16x16x32_bf16 v[18:21], v[134:137], v[226:229], v[18:21]
	v_mfma_f32_16x16x32_bf16 v[2:5], v[150:153], v[226:229], v[2:5]
	s_setprio 0
	s_setprio 1
	v_mfma_f32_16x16x32_bf16 v[62:65], v[172:175], v[188:191], 0
	v_mfma_f32_16x16x32_bf16 v[46:49], v[180:183], v[188:191], 0
	v_mfma_f32_16x16x32_bf16 v[58:61], v[172:175], v[206:209], 0
	v_mfma_f32_16x16x32_bf16 v[42:45], v[180:183], v[206:209], 0
	v_mfma_f32_16x16x32_bf16 v[30:33], v[172:175], v[214:217], 0
	v_mfma_f32_16x16x32_bf16 v[14:17], v[180:183], v[214:217], 0
	v_mfma_f32_16x16x32_bf16 v[26:29], v[172:175], v[222:225], 0
	v_mfma_f32_16x16x32_bf16 v[10:13], v[180:183], v[222:225], 0
	v_mfma_f32_16x16x32_bf16 v[62:65], v[176:179], v[202:205], v[62:65]
	v_mfma_f32_16x16x32_bf16 v[46:49], v[184:187], v[202:205], v[46:49]
	v_mfma_f32_16x16x32_bf16 v[58:61], v[176:179], v[210:213], v[58:61]
	v_mfma_f32_16x16x32_bf16 v[42:45], v[184:187], v[210:213], v[42:45]
	v_mfma_f32_16x16x32_bf16 v[30:33], v[176:179], v[218:221], v[30:33]
	v_mfma_f32_16x16x32_bf16 v[14:17], v[184:187], v[218:221], v[14:17]
	v_mfma_f32_16x16x32_bf16 v[26:29], v[176:179], v[226:229], v[26:29]
	v_mfma_f32_16x16x32_bf16 v[10:13], v[184:187], v[226:229], v[10:13]
	s_setprio 0
	s_barrier
	v_add_u32_e32 v0, 0x18000, v170
	ds_read_b128 v[130:133], v0
	ds_read_b128 v[134:137], v0 offset:1024
	ds_read_b128 v[138:141], v0 offset:2048
	ds_read_b128 v[150:153], v0 offset:3072
	v_add_u32_e32 v0, 0x1c000, v170
	ds_read_b128 v[172:175], v0
	ds_read_b128 v[176:179], v0 offset:1024
	ds_read_b128 v[180:183], v0 offset:2048
	ds_read_b128 v[184:187], v0 offset:3072
	s_add_i32 s16, s16, 0x80000
	s_mov_b32 m0, s73
	ds_read_b128 v[188:191], v171 offset:32768
	ds_read_b128 v[202:205], v171 offset:33792
	ds_read_b128 v[206:209], v171 offset:34816
	ds_read_b128 v[210:213], v171 offset:35840
	ds_read_b128 v[214:217], v171 offset:36864
	ds_read_b128 v[218:221], v171 offset:37888
	ds_read_b128 v[222:225], v171 offset:38912
	ds_read_b128 v[226:229], v171 offset:39936
	buffer_load_dwordx4 v145, s[88:91], s16 offen lds
	s_mov_b32 m0, s74
	s_nop 0
	buffer_load_dwordx4 v167, s[88:91], s16 offen lds
	s_waitcnt vmcnt(8)
	s_waitcnt lgkmcnt(0)
	s_barrier
	s_setprio 1
	s_waitcnt lgkmcnt(7)
	v_mfma_f32_16x16x32_bf16 v[118:121], v[130:133], v[188:191], v[118:121]
	v_mfma_f32_16x16x32_bf16 v[102:105], v[138:141], v[188:191], v[102:105]
	s_waitcnt lgkmcnt(5)
	v_mfma_f32_16x16x32_bf16 v[114:117], v[130:133], v[206:209], v[114:117]
	v_mfma_f32_16x16x32_bf16 v[98:101], v[138:141], v[206:209], v[98:101]
	s_waitcnt lgkmcnt(3)
	v_mfma_f32_16x16x32_bf16 v[86:89], v[130:133], v[214:217], v[86:89]
	v_mfma_f32_16x16x32_bf16 v[70:73], v[138:141], v[214:217], v[70:73]
	s_waitcnt lgkmcnt(1)
	v_mfma_f32_16x16x32_bf16 v[82:85], v[130:133], v[222:225], v[82:85]
	v_mfma_f32_16x16x32_bf16 v[66:69], v[138:141], v[222:225], v[66:69]
	v_mfma_f32_16x16x32_bf16 v[118:121], v[134:137], v[202:205], v[118:121]
	v_mfma_f32_16x16x32_bf16 v[102:105], v[150:153], v[202:205], v[102:105]
	v_mfma_f32_16x16x32_bf16 v[114:117], v[134:137], v[210:213], v[114:117]
	v_mfma_f32_16x16x32_bf16 v[98:101], v[150:153], v[210:213], v[98:101]
	v_mfma_f32_16x16x32_bf16 v[86:89], v[134:137], v[218:221], v[86:89]
	v_mfma_f32_16x16x32_bf16 v[70:73], v[150:153], v[218:221], v[70:73]
	s_waitcnt lgkmcnt(0)
	v_mfma_f32_16x16x32_bf16 v[82:85], v[134:137], v[226:229], v[82:85]
	v_mfma_f32_16x16x32_bf16 v[66:69], v[150:153], v[226:229], v[66:69]
	s_setprio 0
	s_setprio 1
	v_mfma_f32_16x16x32_bf16 v[126:129], v[172:175], v[188:191], v[126:129]
	v_mfma_f32_16x16x32_bf16 v[110:113], v[180:183], v[188:191], v[110:113]
	v_mfma_f32_16x16x32_bf16 v[122:125], v[172:175], v[206:209], v[122:125]
	v_mfma_f32_16x16x32_bf16 v[106:109], v[180:183], v[206:209], v[106:109]
	v_mfma_f32_16x16x32_bf16 v[94:97], v[172:175], v[214:217], v[94:97]
	v_mfma_f32_16x16x32_bf16 v[78:81], v[180:183], v[214:217], v[78:81]
	v_mfma_f32_16x16x32_bf16 v[90:93], v[172:175], v[222:225], v[90:93]
	v_mfma_f32_16x16x32_bf16 v[74:77], v[180:183], v[222:225], v[74:77]
	v_mfma_f32_16x16x32_bf16 v[126:129], v[176:179], v[202:205], v[126:129]
	v_mfma_f32_16x16x32_bf16 v[110:113], v[184:187], v[202:205], v[110:113]
	v_mfma_f32_16x16x32_bf16 v[122:125], v[176:179], v[210:213], v[122:125]
	v_mfma_f32_16x16x32_bf16 v[106:109], v[184:187], v[210:213], v[106:109]
	v_mfma_f32_16x16x32_bf16 v[94:97], v[176:179], v[218:221], v[94:97]
	v_mfma_f32_16x16x32_bf16 v[78:81], v[184:187], v[218:221], v[78:81]
	v_mfma_f32_16x16x32_bf16 v[90:93], v[176:179], v[226:229], v[90:93]
	v_mfma_f32_16x16x32_bf16 v[74:77], v[184:187], v[226:229], v[74:77]
	s_setprio 0
	s_barrier
; #define PG8_STAGEA(bufoff, soff, voff) do { _Pragma("unroll") for (int _i = 0; _i < 2; ++_i) \
;         __builtin_amdgcn_raw_ptr_buffer_load_lds(rsA, (PG8_LAS unsigned*)(lds + (bufoff) + ldsw + _i * 8192), 16, (voff)[_i], (soff), 0, 0); } while (0)
; #define PG8_STAGEB(bufoff, soff, voff) do { _Pragma("unroll") for (int _i = 0; _i < 2; ++_i) \
;         __builtin_amdgcn_raw_ptr_buffer_load_lds(rsB, (PG8_LAS unsigned*)(lds + (bufoff) + ldsw + _i * 8192), 16, (voff)[_i], (soff), 0, 0); } while (0)
; #define PG8_LDA(dst, b, h) do { _Pragma("unroll") for (int m = 0; m < 4; ++m) _Pragma("unroll") for (int k = 0; k < 2; ++k) dst[m][k] = *(const PG8_LAS bf16x8*)(lds + PG8_SA(b, h) + aoff + m * 2048 + k * 1024); } while (0)
; #define PG8_MMA(ai, bj, At, Bt) do { __builtin_amdgcn_s_setprio(1); _Pragma("unroll") for (int m = 0; m < 4; ++m) _Pragma("unroll") for (int n = 0; n < 2; ++n) _Pragma("unroll") for (int k = 0; k < 2; ++k) \
;         acc[ai][bj][m][n] = __builtin_amdgcn_mfma_f32_16x16x32_bf16(Bt[n][k], At[m][k], acc[ai][bj][m][n], 0, 0, 0); __builtin_amdgcn_s_setprio(0); } while (0)
; #define PG8_WAIT_V(n) asm volatile("s_waitcnt vmcnt(" #n ")" ::: "memory")
; #define PG8_WAIT_L(n) asm volatile("s_waitcnt lgkmcnt(" #n ")" ::: "memory")
; #define PG8_BAR __builtin_amdgcn_s_barrier()
; #define PG8_SCHED __builtin_amdgcn_sched_barrier(0)
; template <class Epi, class Sched, bool ALIGN_EPI = false>
; __device__ __forceinline__ void gemm_phase(PG8_LAS unsigned char* lds, const Gemm g, const Sched& S, const Epi& E, const int tid) {
;     ...
;             PG8_LDA(At, 1, 1); PG8_STAGEB(PG8_SB(1, 0), b3, voffB); PG8_STAGEB(PG8_SB(1, 1), b3 + hstepB, voffB); PG8_STAGEA(PG8_SA(1, 0), a3, voffA);
;             PG8_WAIT_V(8); PG8_WAIT_L(0); PG8_BAR; PG8_MMA(1, 0, At, B0); PG8_MMA(1, 1, At, B1); PG8_BAR; PG8_SCHED;
	s_mov_b32 m0, s75
	s_or_b32 s16, s15, 0x80
	ds_read_b128 v[188:191], v171 offset:49152
	ds_read_b128 v[202:205], v171 offset:50176
	ds_read_b128 v[206:209], v171 offset:51200
	ds_read_b128 v[210:213], v171 offset:52224
	ds_read_b128 v[214:217], v171 offset:53248
	ds_read_b128 v[218:221], v171 offset:54272
	ds_read_b128 v[222:225], v171 offset:55296
	ds_read_b128 v[226:229], v171 offset:56320
	buffer_load_dwordx4 v166, s[48:51], s16 offen lds
	s_mov_b32 m0, s76
	s_add_i32 s15, s15, 0x80080
	buffer_load_dwordx4 v168, s[48:51], s16 offen lds
	s_mov_b32 m0, s79
	s_nop 0
	buffer_load_dwordx4 v166, s[48:51], s15 offen lds
	s_mov_b32 m0, s86
	s_nop 0
	buffer_load_dwordx4 v168, s[48:51], s15 offen lds
	s_mov_b32 m0, s77
	s_nop 0
	buffer_load_dwordx4 v145, s[88:91], s14 offen lds
	s_mov_b32 m0, s78
	s_nop 0
	buffer_load_dwordx4 v167, s[88:91], s14 offen lds
	s_waitcnt vmcnt(8)
	s_waitcnt lgkmcnt(0)
	s_barrier
	s_setprio 1
	s_waitcnt lgkmcnt(7)
	v_mfma_f32_16x16x32_bf16 v[54:57], v[130:133], v[188:191], v[54:57]
	v_mfma_f32_16x16x32_bf16 v[38:41], v[138:141], v[188:191], v[38:41]
	s_waitcnt lgkmcnt(5)
	v_mfma_f32_16x16x32_bf16 v[50:53], v[130:133], v[206:209], v[50:53]
	v_mfma_f32_16x16x32_bf16 v[34:37], v[138:141], v[206:209], v[34:37]
	s_waitcnt lgkmcnt(3)
	v_mfma_f32_16x16x32_bf16 v[22:25], v[130:133], v[214:217], v[22:25]
	v_mfma_f32_16x16x32_bf16 v[6:9], v[138:141], v[214:217], v[6:9]
	s_waitcnt lgkmcnt(1)
	v_mfma_f32_16x16x32_bf16 v[18:21], v[130:133], v[222:225], v[18:21]
	v_mfma_f32_16x16x32_bf16 v[2:5], v[138:141], v[222:225], v[2:5]
	v_mfma_f32_16x16x32_bf16 v[54:57], v[134:137], v[202:205], v[54:57]
	v_mfma_f32_16x16x32_bf16 v[38:41], v[150:153], v[202:205], v[38:41]
	v_mfma_f32_16x16x32_bf16 v[50:53], v[134:137], v[210:213], v[50:53]
	v_mfma_f32_16x16x32_bf16 v[34:37], v[150:153], v[210:213], v[34:37]
	v_mfma_f32_16x16x32_bf16 v[22:25], v[134:137], v[218:221], v[22:25]
	v_mfma_f32_16x16x32_bf16 v[6:9], v[150:153], v[218:221], v[6:9]
	s_waitcnt lgkmcnt(0)
	v_mfma_f32_16x16x32_bf16 v[18:21], v[134:137], v[226:229], v[18:21]
	v_mfma_f32_16x16x32_bf16 v[2:5], v[150:153], v[226:229], v[2:5]
	s_setprio 0
	s_setprio 1
	v_mfma_f32_16x16x32_bf16 v[62:65], v[172:175], v[188:191], v[62:65]
	v_mfma_f32_16x16x32_bf16 v[46:49], v[180:183], v[188:191], v[46:49]
	v_mfma_f32_16x16x32_bf16 v[58:61], v[172:175], v[206:209], v[58:61]
	v_mfma_f32_16x16x32_bf16 v[42:45], v[180:183], v[206:209], v[42:45]
	v_mfma_f32_16x16x32_bf16 v[30:33], v[172:175], v[214:217], v[30:33]
	v_mfma_f32_16x16x32_bf16 v[14:17], v[180:183], v[214:217], v[14:17]
	v_mfma_f32_16x16x32_bf16 v[26:29], v[172:175], v[222:225], v[26:29]
	v_mfma_f32_16x16x32_bf16 v[10:13], v[180:183], v[222:225], v[10:13]
	v_mfma_f32_16x16x32_bf16 v[62:65], v[176:179], v[202:205], v[62:65]
	v_mfma_f32_16x16x32_bf16 v[46:49], v[184:187], v[202:205], v[46:49]
	v_mfma_f32_16x16x32_bf16 v[58:61], v[176:179], v[210:213], v[58:61]
	v_mfma_f32_16x16x32_bf16 v[42:45], v[184:187], v[210:213], v[42:45]
	v_mfma_f32_16x16x32_bf16 v[30:33], v[176:179], v[218:221], v[30:33]
	v_mfma_f32_16x16x32_bf16 v[14:17], v[184:187], v[218:221], v[14:17]
	v_mfma_f32_16x16x32_bf16 v[26:29], v[176:179], v[226:229], v[26:29]
	v_mfma_f32_16x16x32_bf16 v[10:13], v[184:187], v[226:229], v[10:13]
	s_setprio 0
	s_barrier
	s_add_i32 s13, s13, 2
	s_addk_i32 s1, 0x100
	s_addk_i32 s12, 0x100
	s_cmp_gt_u32 s13, 29

; #define PG8_STAGEA(bufoff, soff, voff) do { _Pragma("unroll") for (int _i = 0; _i < 2; ++_i) \
;         __builtin_amdgcn_raw_ptr_buffer_load_lds(rsA, (PG8_LAS unsigned*)(lds + (bufoff) + ldsw + _i * 8192), 16, (voff)[_i], (soff), 0, 0); } while (0)
; #define PG8_STAGEB(bufoff, soff, voff) do { _Pragma("unroll") for (int _i = 0; _i < 2; ++_i) \
;         __builtin_amdgcn_raw_ptr_buffer_load_lds(rsB, (PG8_LAS unsigned*)(lds + (bufoff) + ldsw + _i * 8192), 16, (voff)[_i], (soff), 0, 0); } while (0)
; #define PG8_LDA(dst, b, h) do { _Pragma("unroll") for (int m = 0; m < 4; ++m) _Pragma("unroll") for (int k = 0; k < 2; ++k) dst[m][k] = *(const PG8_LAS bf16x8*)(lds + PG8_SA(b, h) + aoff + m * 2048 + k * 1024); } while (0)
; #define PG8_LDB(dst, b, h) do { _Pragma("unroll") for (int n = 0; n < 2; ++n) _Pragma("unroll") for (int k = 0; k < 2; ++k) dst[n][k] = *(const PG8_LAS bf16x8*)(lds + PG8_SB(b, h) + boff + n * 2048 + k * 1024); } while (0)
; #define PG8_MMA(ai, bj, At, Bt) do { __builtin_amdgcn_s_setprio(1); _Pragma("unroll") for (int m = 0; m < 4; ++m) _Pragma("unroll") for (int n = 0; n < 2; ++n) _Pragma("unroll") for (int k = 0; k < 2; ++k) \
;         acc[ai][bj][m][n] = __builtin_amdgcn_mfma_f32_16x16x32_bf16(Bt[n][k], At[m][k], acc[ai][bj][m][n], 0, 0, 0); __builtin_amdgcn_s_setprio(0); } while (0)
; #define PG8_BAR __builtin_amdgcn_s_barrier()
; template <class Epi, class Sched, bool ALIGN_EPI = false>
; __device__ __forceinline__ void gemm_phase(PG8_LAS unsigned char* lds, const Gemm g, const Sched& S, const Epi& E, const int tid) {
;     ...
;             PG8_LDB(B0, 0, 0); PG8_LDB(B1, 0, 1); PG8_SCHED; PG8_LDA(At, 0, 0); PG8_STAGEA(PG8_SA(1, 1), a1 + hstepA, voffA);
;             PG8_WAIT_V(8); PG8_WAIT_L(0); PG8_BAR; PG8_MMA(0, 0, At, B0); PG8_MMA(0, 1, At, B1); PG8_BAR; PG8_SCHED;
;             PG8_LDA(At, 0, 1); PG8_STAGEB(PG8_SB(0, 0), b2, voffB); PG8_STAGEB(PG8_SB(0, 1), b2 + hstepB, voffB); PG8_STAGEA(PG8_SA(0, 0), a2, voffA);
;             PG8_WAIT_V(8); PG8_WAIT_L(0); PG8_BAR; PG8_MMA(1, 0, At, B0); PG8_MMA(1, 1, At, B1); PG8_BAR; PG8_SCHED;
;     ...
; #pragma unroll
;         for (int a = 0; a < 2; ++a)
; #pragma unroll
;             for (int b = 0; b < 2; ++b)
; #pragma unroll
;                 for (int m = 0; m < 4; ++m)
; #pragma unroll
;                     for (int n = 0; n < 2; ++n) acc[a][b][m][n] = (f32x4){0.f, 0.f, 0.f, 0.f};
.LBB0_950:
	s_add_i32 s28, s61, 0x80
	s_add_i32 s29, s60, 0x100
	s_mov_b32 s42, 0
	s_waitcnt vmcnt(23)
	s_waitcnt vmcnt(21)
	s_waitcnt vmcnt(20)
	s_waitcnt vmcnt(19)
	s_waitcnt vmcnt(18)
	s_waitcnt vmcnt(17)
	s_waitcnt vmcnt(15)
	s_waitcnt vmcnt(14)
	v_add_u32_e32 v86, 0x10000, v177
	v_add_u32_e32 v168, 0x14000, v177
	ds_read_b128 v[74:77], v86
	ds_read_b128 v[78:81], v86 offset:1024
	ds_read_b128 v[82:85], v86 offset:2048
	ds_read_b128 v[86:89], v86 offset:3072
	ds_read_b128 v[146:149], v168
	ds_read_b128 v[150:153], v168 offset:1024
	ds_read_b128 v[164:167], v168 offset:2048
	ds_read_b128 v[168:171], v168 offset:3072
	s_add_i32 s43, s28, 0x80
	s_cmp_eq_u32 s51, s42
	s_cselect_b32 s61, s56, s43
	s_cselect_b32 s60, s57, s29
	s_add_i32 s43, s61, 0x80
	s_add_i32 s46, s11, s28
	s_mov_b32 m0, s52
	ds_read_b128 v[180:183], v178
	ds_read_b128 v[184:187], v178 offset:1024
	ds_read_b128 v[188:191], v178 offset:2048
	ds_read_b128 v[202:205], v178 offset:3072
	ds_read_b128 v[206:209], v178 offset:4096
	ds_read_b128 v[210:213], v178 offset:5120
	ds_read_b128 v[214:217], v178 offset:6144
	ds_read_b128 v[218:221], v178 offset:7168
	buffer_load_dwordx4 v0, s[88:91], s46 offen lds
	s_mov_b32 m0, s53
	s_nop 0
	buffer_load_dwordx4 v173, s[88:91], s46 offen lds
	s_waitcnt vmcnt(8)
	s_waitcnt lgkmcnt(0)
	s_barrier
	s_setprio 1
	s_waitcnt lgkmcnt(7)
	v_mfma_f32_16x16x32_bf16 v[142:145], v[74:77], v[180:183], 0
	v_mfma_f32_16x16x32_bf16 v[138:141], v[82:85], v[180:183], 0
	s_waitcnt lgkmcnt(5)
	v_mfma_f32_16x16x32_bf16 v[126:129], v[74:77], v[188:191], 0
	v_mfma_f32_16x16x32_bf16 v[122:125], v[82:85], v[188:191], 0
	s_waitcnt lgkmcnt(3)
	v_mfma_f32_16x16x32_bf16 v[110:113], v[74:77], v[206:209], 0
	v_mfma_f32_16x16x32_bf16 v[106:109], v[82:85], v[206:209], 0
	s_waitcnt lgkmcnt(1)
	v_mfma_f32_16x16x32_bf16 v[94:97], v[74:77], v[214:217], 0
	v_mfma_f32_16x16x32_bf16 v[90:93], v[82:85], v[214:217], 0
	v_mfma_f32_16x16x32_bf16 v[142:145], v[78:81], v[184:187], v[142:145]
	v_mfma_f32_16x16x32_bf16 v[138:141], v[86:89], v[184:187], v[138:141]
	v_mfma_f32_16x16x32_bf16 v[126:129], v[78:81], v[202:205], v[126:129]
	v_mfma_f32_16x16x32_bf16 v[122:125], v[86:89], v[202:205], v[122:125]
	v_mfma_f32_16x16x32_bf16 v[110:113], v[78:81], v[210:213], v[110:113]
	v_mfma_f32_16x16x32_bf16 v[106:109], v[86:89], v[210:213], v[106:109]
	s_waitcnt lgkmcnt(0)
	v_mfma_f32_16x16x32_bf16 v[94:97], v[78:81], v[218:221], v[94:97]
	v_mfma_f32_16x16x32_bf16 v[90:93], v[86:89], v[218:221], v[90:93]
	s_setprio 0
	s_setprio 1
	v_mfma_f32_16x16x32_bf16 v[134:137], v[146:149], v[180:183], 0
	v_mfma_f32_16x16x32_bf16 v[130:133], v[164:167], v[180:183], 0
	v_mfma_f32_16x16x32_bf16 v[118:121], v[146:149], v[188:191], 0
	v_mfma_f32_16x16x32_bf16 v[114:117], v[164:167], v[188:191], 0
	v_mfma_f32_16x16x32_bf16 v[102:105], v[146:149], v[206:209], 0
	v_mfma_f32_16x16x32_bf16 v[98:101], v[164:167], v[206:209], 0
	v_mfma_f32_16x16x32_bf16 v[70:73], v[146:149], v[214:217], 0
	v_mfma_f32_16x16x32_bf16 v[66:69], v[164:167], v[214:217], 0
	v_mfma_f32_16x16x32_bf16 v[134:137], v[150:153], v[184:187], v[134:137]
	v_mfma_f32_16x16x32_bf16 v[130:133], v[168:171], v[184:187], v[130:133]
	v_mfma_f32_16x16x32_bf16 v[118:121], v[150:153], v[202:205], v[118:121]
	v_mfma_f32_16x16x32_bf16 v[114:117], v[168:171], v[202:205], v[114:117]
	v_mfma_f32_16x16x32_bf16 v[102:105], v[150:153], v[210:213], v[102:105]
	v_mfma_f32_16x16x32_bf16 v[98:101], v[168:171], v[210:213], v[98:101]
	v_mfma_f32_16x16x32_bf16 v[70:73], v[150:153], v[218:221], v[70:73]
	v_mfma_f32_16x16x32_bf16 v[66:69], v[168:171], v[218:221], v[66:69]
	s_setprio 0
	s_barrier
	s_mov_b32 m0, s17
	s_mov_b32 s46, s90
	s_mov_b32 s47, s91
	ds_read_b128 v[180:183], v178 offset:16384
	ds_read_b128 v[184:187], v178 offset:17408
	ds_read_b128 v[188:191], v178 offset:18432
	ds_read_b128 v[202:205], v178 offset:19456
	ds_read_b128 v[206:209], v178 offset:20480
	ds_read_b128 v[210:213], v178 offset:21504
	ds_read_b128 v[214:217], v178 offset:22528
	ds_read_b128 v[218:221], v178 offset:23552
	buffer_load_dwordx4 v172, s[44:47], s60 offen lds
	s_mov_b32 m0, s20
	s_add_i32 s62, s60, s14
	buffer_load_dwordx4 v174, s[44:47], s60 offen lds
	s_mov_b32 m0, s21
	s_nop 0
	buffer_load_dwordx4 v172, s[44:47], s62 offen lds
	s_mov_b32 m0, s24
	s_nop 0
	buffer_load_dwordx4 v174, s[44:47], s62 offen lds
	s_mov_b32 m0, s16
	s_nop 0
	buffer_load_dwordx4 v0, s[88:91], s61 offen lds
	s_mov_b32 m0, s25
	s_nop 0
	buffer_load_dwordx4 v173, s[88:91], s61 offen lds
	s_waitcnt vmcnt(8)
	s_waitcnt lgkmcnt(0)
	s_barrier
; #define PG8_STAGEA(bufoff, soff, voff) do { _Pragma("unroll") for (int _i = 0; _i < 2; ++_i) \
;         __builtin_amdgcn_raw_ptr_buffer_load_lds(rsA, (PG8_LAS unsigned*)(lds + (bufoff) + ldsw + _i * 8192), 16, (voff)[_i], (soff), 0, 0); } while (0)
; #define PG8_STAGEB(bufoff, soff, voff) do { _Pragma("unroll") for (int _i = 0; _i < 2; ++_i) \
;         __builtin_amdgcn_raw_ptr_buffer_load_lds(rsB, (PG8_LAS unsigned*)(lds + (bufoff) + ldsw + _i * 8192), 16, (voff)[_i], (soff), 0, 0); } while (0)
; #define PG8_LDA(dst, b, h) do { _Pragma("unroll") for (int m = 0; m < 4; ++m) _Pragma("unroll") for (int k = 0; k < 2; ++k) dst[m][k] = *(const PG8_LAS bf16x8*)(lds + PG8_SA(b, h) + aoff + m * 2048 + k * 1024); } while (0)
; #define PG8_LDB(dst, b, h) do { _Pragma("unroll") for (int n = 0; n < 2; ++n) _Pragma("unroll") for (int k = 0; k < 2; ++k) dst[n][k] = *(const PG8_LAS bf16x8*)(lds + PG8_SB(b, h) + boff + n * 2048 + k * 1024); } while (0)
; #define PG8_MMA(ai, bj, At, Bt) do { __builtin_amdgcn_s_setprio(1); _Pragma("unroll") for (int m = 0; m < 4; ++m) _Pragma("unroll") for (int n = 0; n < 2; ++n) _Pragma("unroll") for (int k = 0; k < 2; ++k) \
;         acc[ai][bj][m][n] = __builtin_amdgcn_mfma_f32_16x16x32_bf16(Bt[n][k], At[m][k], acc[ai][bj][m][n], 0, 0, 0); __builtin_amdgcn_s_setprio(0); } while (0)
; #define PG8_WAIT_V(n) asm volatile("s_waitcnt vmcnt(" #n ")" ::: "memory")
; #define PG8_WAIT_L(n) asm volatile("s_waitcnt lgkmcnt(" #n ")" ::: "memory")
; #define PG8_BAR __builtin_amdgcn_s_barrier()
; template <class Epi, class Sched, bool ALIGN_EPI = false>
; __device__ __forceinline__ void gemm_phase(PG8_LAS unsigned char* lds, const Gemm g, const Sched& S, const Epi& E, const int tid) {
;     ...
;             PG8_WAIT_V(8); PG8_WAIT_L(0); PG8_BAR; PG8_MMA(0, 0, At, B0); PG8_MMA(0, 1, At, B1); PG8_BAR; PG8_SCHED;
;             PG8_LDA(At, 0, 1); PG8_STAGEB(PG8_SB(0, 0), b2, voffB); PG8_STAGEB(PG8_SB(0, 1), b2 + hstepB, voffB); PG8_STAGEA(PG8_SA(0, 0), a2, voffA);
;             PG8_WAIT_V(8); PG8_WAIT_L(0); PG8_BAR; PG8_MMA(1, 0, At, B0); PG8_MMA(1, 1, At, B1); PG8_BAR; PG8_SCHED;
;             PG8_LDB(B0, 1, 0); PG8_LDB(B1, 1, 1); PG8_SCHED; PG8_LDA(At, 1, 0); PG8_STAGEA(PG8_SA(0, 1), a2 + hstepA, voffA);
;             PG8_WAIT_V(8); PG8_WAIT_L(0); PG8_BAR; PG8_MMA(0, 0, At, B0); PG8_MMA(0, 1, At, B1); PG8_BAR; PG8_SCHED;
	s_setprio 1
	s_waitcnt lgkmcnt(7)
	v_mfma_f32_16x16x32_bf16 v[62:65], v[74:77], v[180:183], 0
	v_mfma_f32_16x16x32_bf16 v[58:61], v[82:85], v[180:183], 0
	s_waitcnt lgkmcnt(5)
	v_mfma_f32_16x16x32_bf16 v[46:49], v[74:77], v[188:191], 0
	v_mfma_f32_16x16x32_bf16 v[42:45], v[82:85], v[188:191], 0
	s_waitcnt lgkmcnt(3)
	v_mfma_f32_16x16x32_bf16 v[30:33], v[74:77], v[206:209], 0
	v_mfma_f32_16x16x32_bf16 v[26:29], v[82:85], v[206:209], 0
	s_waitcnt lgkmcnt(1)
	v_mfma_f32_16x16x32_bf16 v[14:17], v[74:77], v[214:217], 0
	v_mfma_f32_16x16x32_bf16 v[10:13], v[82:85], v[214:217], 0
	v_mfma_f32_16x16x32_bf16 v[62:65], v[78:81], v[184:187], v[62:65]
	v_mfma_f32_16x16x32_bf16 v[58:61], v[86:89], v[184:187], v[58:61]
	v_mfma_f32_16x16x32_bf16 v[46:49], v[78:81], v[202:205], v[46:49]
	v_mfma_f32_16x16x32_bf16 v[42:45], v[86:89], v[202:205], v[42:45]
	v_mfma_f32_16x16x32_bf16 v[30:33], v[78:81], v[210:213], v[30:33]
	v_mfma_f32_16x16x32_bf16 v[26:29], v[86:89], v[210:213], v[26:29]
	s_waitcnt lgkmcnt(0)
	v_mfma_f32_16x16x32_bf16 v[14:17], v[78:81], v[218:221], v[14:17]
	v_mfma_f32_16x16x32_bf16 v[10:13], v[86:89], v[218:221], v[10:13]
	s_setprio 0
	s_setprio 1
	v_mfma_f32_16x16x32_bf16 v[54:57], v[146:149], v[180:183], 0
	v_mfma_f32_16x16x32_bf16 v[50:53], v[164:167], v[180:183], 0
	v_mfma_f32_16x16x32_bf16 v[38:41], v[146:149], v[188:191], 0
	v_mfma_f32_16x16x32_bf16 v[34:37], v[164:167], v[188:191], 0
	v_mfma_f32_16x16x32_bf16 v[22:25], v[146:149], v[206:209], 0
	v_mfma_f32_16x16x32_bf16 v[18:21], v[164:167], v[206:209], 0
	v_mfma_f32_16x16x32_bf16 v[6:9], v[146:149], v[214:217], 0
	v_mfma_f32_16x16x32_bf16 v[2:5], v[164:167], v[214:217], 0
	v_mfma_f32_16x16x32_bf16 v[54:57], v[150:153], v[184:187], v[54:57]
	v_mfma_f32_16x16x32_bf16 v[50:53], v[168:171], v[184:187], v[50:53]
	v_mfma_f32_16x16x32_bf16 v[38:41], v[150:153], v[202:205], v[38:41]
	v_mfma_f32_16x16x32_bf16 v[34:37], v[168:171], v[202:205], v[34:37]
	v_mfma_f32_16x16x32_bf16 v[22:25], v[150:153], v[210:213], v[22:25]
	v_mfma_f32_16x16x32_bf16 v[18:21], v[168:171], v[210:213], v[18:21]
	v_mfma_f32_16x16x32_bf16 v[6:9], v[150:153], v[218:221], v[6:9]
	v_mfma_f32_16x16x32_bf16 v[2:5], v[168:171], v[218:221], v[2:5]
	s_setprio 0
	s_barrier
	v_add_u32_e32 v86, 0x18000, v177
	v_add_u32_e32 v168, 0x1c000, v177
	ds_read_b128 v[74:77], v86
	ds_read_b128 v[78:81], v86 offset:1024
	ds_read_b128 v[82:85], v86 offset:2048
	ds_read_b128 v[86:89], v86 offset:3072
	ds_read_b128 v[146:149], v168
	ds_read_b128 v[150:153], v168 offset:1024
	ds_read_b128 v[164:167], v168 offset:2048
	ds_read_b128 v[168:171], v168 offset:3072
	s_add_i32 s61, s61, s11
	s_mov_b32 m0, s30
	ds_read_b128 v[180:183], v178 offset:32768
	ds_read_b128 v[184:187], v178 offset:33792
	ds_read_b128 v[188:191], v178 offset:34816
	ds_read_b128 v[202:205], v178 offset:35840
	ds_read_b128 v[206:209], v178 offset:36864
	ds_read_b128 v[210:213], v178 offset:37888
	ds_read_b128 v[214:217], v178 offset:38912
	ds_read_b128 v[218:221], v178 offset:39936
	buffer_load_dwordx4 v0, s[88:91], s61 offen lds
	s_mov_b32 m0, s31
	s_nop 0
	buffer_load_dwordx4 v173, s[88:91], s61 offen lds
	s_waitcnt vmcnt(8)
	s_waitcnt lgkmcnt(0)
	s_barrier
	s_setprio 1
	s_waitcnt lgkmcnt(7)
	v_mfma_f32_16x16x32_bf16 v[142:145], v[74:77], v[180:183], v[142:145]
	v_mfma_f32_16x16x32_bf16 v[138:141], v[82:85], v[180:183], v[138:141]
	s_waitcnt lgkmcnt(5)
	v_mfma_f32_16x16x32_bf16 v[126:129], v[74:77], v[188:191], v[126:129]
	v_mfma_f32_16x16x32_bf16 v[122:125], v[82:85], v[188:191], v[122:125]
	s_waitcnt lgkmcnt(3)
	v_mfma_f32_16x16x32_bf16 v[110:113], v[74:77], v[206:209], v[110:113]
	v_mfma_f32_16x16x32_bf16 v[106:109], v[82:85], v[206:209], v[106:109]
	s_waitcnt lgkmcnt(1)
	v_mfma_f32_16x16x32_bf16 v[94:97], v[74:77], v[214:217], v[94:97]
	v_mfma_f32_16x16x32_bf16 v[90:93], v[82:85], v[214:217], v[90:93]
	v_mfma_f32_16x16x32_bf16 v[142:145], v[78:81], v[184:187], v[142:145]
	v_mfma_f32_16x16x32_bf16 v[138:141], v[86:89], v[184:187], v[138:141]
	v_mfma_f32_16x16x32_bf16 v[126:129], v[78:81], v[202:205], v[126:129]
	v_mfma_f32_16x16x32_bf16 v[122:125], v[86:89], v[202:205], v[122:125]
	v_mfma_f32_16x16x32_bf16 v[110:113], v[78:81], v[210:213], v[110:113]
	v_mfma_f32_16x16x32_bf16 v[106:109], v[86:89], v[210:213], v[106:109]
	s_waitcnt lgkmcnt(0)
	v_mfma_f32_16x16x32_bf16 v[94:97], v[78:81], v[218:221], v[94:97]
	v_mfma_f32_16x16x32_bf16 v[90:93], v[86:89], v[218:221], v[90:93]
	s_setprio 0
	s_setprio 1
	v_mfma_f32_16x16x32_bf16 v[134:137], v[146:149], v[180:183], v[134:137]
	v_mfma_f32_16x16x32_bf16 v[130:133], v[164:167], v[180:183], v[130:133]
	v_mfma_f32_16x16x32_bf16 v[118:121], v[146:149], v[188:191], v[118:121]
	v_mfma_f32_16x16x32_bf16 v[114:117], v[164:167], v[188:191], v[114:117]
	v_mfma_f32_16x16x32_bf16 v[102:105], v[146:149], v[206:209], v[102:105]
	v_mfma_f32_16x16x32_bf16 v[98:101], v[164:167], v[206:209], v[98:101]
	v_mfma_f32_16x16x32_bf16 v[70:73], v[146:149], v[214:217], v[70:73]
	v_mfma_f32_16x16x32_bf16 v[66:69], v[164:167], v[214:217], v[66:69]
	v_mfma_f32_16x16x32_bf16 v[134:137], v[150:153], v[184:187], v[134:137]
	v_mfma_f32_16x16x32_bf16 v[130:133], v[168:171], v[184:187], v[130:133]
	v_mfma_f32_16x16x32_bf16 v[118:121], v[150:153], v[202:205], v[118:121]
	v_mfma_f32_16x16x32_bf16 v[114:117], v[168:171], v[202:205], v[114:117]
	v_mfma_f32_16x16x32_bf16 v[102:105], v[150:153], v[210:213], v[102:105]
	v_mfma_f32_16x16x32_bf16 v[98:101], v[168:171], v[210:213], v[98:101]
	v_mfma_f32_16x16x32_bf16 v[70:73], v[150:153], v[218:221], v[70:73]
	v_mfma_f32_16x16x32_bf16 v[66:69], v[168:171], v[218:221], v[66:69]
	s_setprio 0
	s_barrier
; #define PG8_STAGEA(bufoff, soff, voff) do { _Pragma("unroll") for (int _i = 0; _i < 2; ++_i) \
;         __builtin_amdgcn_raw_ptr_buffer_load_lds(rsA, (PG8_LAS unsigned*)(lds + (bufoff) + ldsw + _i * 8192), 16, (voff)[_i], (soff), 0, 0); } while (0)
; #define PG8_STAGEB(bufoff, soff, voff) do { _Pragma("unroll") for (int _i = 0; _i < 2; ++_i) \
;         __builtin_amdgcn_raw_ptr_buffer_load_lds(rsB, (PG8_LAS unsigned*)(lds + (bufoff) + ldsw + _i * 8192), 16, (voff)[_i], (soff), 0, 0); } while (0)
; #define PG8_LDA(dst, b, h) do { _Pragma("unroll") for (int m = 0; m < 4; ++m) _Pragma("unroll") for (int k = 0; k < 2; ++k) dst[m][k] = *(const PG8_LAS bf16x8*)(lds + PG8_SA(b, h) + aoff + m * 2048 + k * 1024); } while (0)
; #define PG8_MMA(ai, bj, At, Bt) do { __builtin_amdgcn_s_setprio(1); _Pragma("unroll") for (int m = 0; m < 4; ++m) _Pragma("unroll") for (int n = 0; n < 2; ++n) _Pragma("unroll") for (int k = 0; k < 2; ++k) \
;         acc[ai][bj][m][n] = __builtin_amdgcn_mfma_f32_16x16x32_bf16(Bt[n][k], At[m][k], acc[ai][bj][m][n], 0, 0, 0); __builtin_amdgcn_s_setprio(0); } while (0)
; #define PG8_WAIT_V(n) asm volatile("s_waitcnt vmcnt(" #n ")" ::: "memory")
; #define PG8_WAIT_L(n) asm volatile("s_waitcnt lgkmcnt(" #n ")" ::: "memory")
; #define PG8_BAR __builtin_amdgcn_s_barrier()
; #define PG8_SCHED __builtin_amdgcn_sched_barrier(0)
; template <class Epi, class Sched, bool ALIGN_EPI = false>
; __device__ __forceinline__ void gemm_phase(PG8_LAS unsigned char* lds, const Gemm g, const Sched& S, const Epi& E, const int tid) {
;     ...
;             PG8_LDA(At, 1, 1); PG8_STAGEB(PG8_SB(1, 0), b3, voffB); PG8_STAGEB(PG8_SB(1, 1), b3 + hstepB, voffB); PG8_STAGEA(PG8_SA(1, 0), a3, voffA);
;             PG8_WAIT_V(8); PG8_WAIT_L(0); PG8_BAR; PG8_MMA(1, 0, At, B0); PG8_MMA(1, 1, At, B1); PG8_BAR; PG8_SCHED;
	s_mov_b32 m0, s33
	s_addk_i32 s60, 0x80
	ds_read_b128 v[180:183], v178 offset:49152
	ds_read_b128 v[184:187], v178 offset:50176
	ds_read_b128 v[188:191], v178 offset:51200
	ds_read_b128 v[202:205], v178 offset:52224
	ds_read_b128 v[206:209], v178 offset:53248
	ds_read_b128 v[210:213], v178 offset:54272
	ds_read_b128 v[214:217], v178 offset:55296
	ds_read_b128 v[218:221], v178 offset:56320
	buffer_load_dwordx4 v172, s[44:47], s60 offen lds
	s_mov_b32 m0, s34
	s_nop 0
	buffer_load_dwordx4 v174, s[44:47], s60 offen lds
	s_add_i32 s60, s60, s14
	s_mov_b32 m0, s37
	s_nop 0
	buffer_load_dwordx4 v172, s[44:47], s60 offen lds
	s_mov_b32 m0, s38
	s_nop 0
	buffer_load_dwordx4 v174, s[44:47], s60 offen lds
	s_mov_b32 m0, s35
	s_nop 0
	buffer_load_dwordx4 v0, s[88:91], s43 offen lds
	s_mov_b32 m0, s36
	s_nop 0
	buffer_load_dwordx4 v173, s[88:91], s43 offen lds
	s_waitcnt vmcnt(8)
	s_waitcnt lgkmcnt(0)
	s_barrier
	s_setprio 1
	s_waitcnt lgkmcnt(7)
	v_mfma_f32_16x16x32_bf16 v[62:65], v[74:77], v[180:183], v[62:65]
	v_mfma_f32_16x16x32_bf16 v[58:61], v[82:85], v[180:183], v[58:61]
	s_waitcnt lgkmcnt(5)
	v_mfma_f32_16x16x32_bf16 v[46:49], v[74:77], v[188:191], v[46:49]
	v_mfma_f32_16x16x32_bf16 v[42:45], v[82:85], v[188:191], v[42:45]
	s_waitcnt lgkmcnt(3)
	v_mfma_f32_16x16x32_bf16 v[30:33], v[74:77], v[206:209], v[30:33]
	v_mfma_f32_16x16x32_bf16 v[26:29], v[82:85], v[206:209], v[26:29]
	s_waitcnt lgkmcnt(1)
	v_mfma_f32_16x16x32_bf16 v[14:17], v[74:77], v[214:217], v[14:17]
	v_mfma_f32_16x16x32_bf16 v[10:13], v[82:85], v[214:217], v[10:13]
	v_mfma_f32_16x16x32_bf16 v[62:65], v[78:81], v[184:187], v[62:65]
	v_mfma_f32_16x16x32_bf16 v[58:61], v[86:89], v[184:187], v[58:61]
	v_mfma_f32_16x16x32_bf16 v[46:49], v[78:81], v[202:205], v[46:49]
	v_mfma_f32_16x16x32_bf16 v[42:45], v[86:89], v[202:205], v[42:45]
	v_mfma_f32_16x16x32_bf16 v[30:33], v[78:81], v[210:213], v[30:33]
	v_mfma_f32_16x16x32_bf16 v[26:29], v[86:89], v[210:213], v[26:29]
	s_waitcnt lgkmcnt(0)
	v_mfma_f32_16x16x32_bf16 v[14:17], v[78:81], v[218:221], v[14:17]
	v_mfma_f32_16x16x32_bf16 v[10:13], v[86:89], v[218:221], v[10:13]
	s_setprio 0
	s_setprio 1
	v_mfma_f32_16x16x32_bf16 v[54:57], v[146:149], v[180:183], v[54:57]
	v_mfma_f32_16x16x32_bf16 v[50:53], v[164:167], v[180:183], v[50:53]
	v_mfma_f32_16x16x32_bf16 v[38:41], v[146:149], v[188:191], v[38:41]
	v_mfma_f32_16x16x32_bf16 v[34:37], v[164:167], v[188:191], v[34:37]
	v_mfma_f32_16x16x32_bf16 v[22:25], v[146:149], v[206:209], v[22:25]
	v_mfma_f32_16x16x32_bf16 v[18:21], v[164:167], v[206:209], v[18:21]
	v_mfma_f32_16x16x32_bf16 v[6:9], v[146:149], v[214:217], v[6:9]
	v_mfma_f32_16x16x32_bf16 v[2:5], v[164:167], v[214:217], v[2:5]
	v_mfma_f32_16x16x32_bf16 v[54:57], v[150:153], v[184:187], v[54:57]
	v_mfma_f32_16x16x32_bf16 v[50:53], v[168:171], v[184:187], v[50:53]
	v_mfma_f32_16x16x32_bf16 v[38:41], v[150:153], v[202:205], v[38:41]
	v_mfma_f32_16x16x32_bf16 v[34:37], v[168:171], v[202:205], v[34:37]
	v_mfma_f32_16x16x32_bf16 v[22:25], v[150:153], v[210:213], v[22:25]
	v_mfma_f32_16x16x32_bf16 v[18:21], v[168:171], v[210:213], v[18:21]
	v_mfma_f32_16x16x32_bf16 v[6:9], v[150:153], v[218:221], v[6:9]
	v_mfma_f32_16x16x32_bf16 v[2:5], v[168:171], v[218:221], v[2:5]
	s_setprio 0
	s_barrier
	s_add_i32 s42, s42, 2
	s_addk_i32 s28, 0x100
	s_addk_i32 s29, 0x100
	s_cmp_ge_u32 s42, s50
